# ln_mid walks the rows of the workgroup's own router half unit; the grid barrier between ln_mid and router becomes a workgroup barrier (grid 256 only)
# speedup vs baseline: 1.0055x; 1.0001x over previous
; DEVI int vtid() { return tidx() & 255; }
; DEVI int vbid() { return bidx() * 2 + vhb(); }
; DEVI int vgrid() { return (int)gridDim.x * 2; }
; DEVI void phase_ln_mid(const Params& p, int l) {
;     const int lane = vtid() & 63, gw = vbid() * 4 + (vtid() >> 6), nw = vgrid() * 4;
;     bf16_t* xab = p.xa; bf16_t* hb = p.h; asm volatile("" : "+s"(xab), "+s"(hb));
;     f32x4 lg4[4], lb4[4], sh4[4], sc4[4]; int bcur = -1;
; #pragma unroll
;     for (int i = 0; i < 4; ++i) { const int c = lane * 4 + 256 * i; lg4[i] = *(const f32x4*)(p.ln1_g + l * 1024 + c); lb4[i] = *(const f32x4*)(p.ln1_b + l * 1024 + c); sh4[i] = lg4[i]; sc4[i] = lg4[i]; }
;     u32x2 rw[4], rn[4];
; #pragma unroll
;     for (int i = 0; i < 4; ++i) rw[i] = *(const u32x2*)(xab + (size_t)(gw < T_ ? gw : 0) * 1024 + lane * 4 + 256 * i);
;     for (int t = gw; t < T_; t += nw) {
.LBB0_1080:
	s_or_b64 exec, exec, s[4:5]
	s_mov_b64 s[8:9], s[0:1]
	v_mov_b32_e32 v34, v0
	s_mov_b32 s2, s84
	s_waitcnt lgkmcnt(0)
	v_mov_b32_e32 v2, v0
	v_mov_b32_e32 v18, v0
	s_barrier
	s_load_dwordx4 s[4:7], s[8:9], 0x160
	v_readfirstlane_b32 s10, v2
	s_lshr_b32 s10, s10, 6
	s_cmpk_lg_u32 s33, 0x100
	s_cbranch_scc1 .Lmy_lnm_old_0
	s_lshr_b32 s12, s2, 1
	s_and_b32 s13, s12, 7
	s_lshl_b32 s13, s13, 4
	s_lshr_b32 s12, s12, 3
	s_add_i32 s12, s12, s13
	s_lshl_b32 s12, s12, 8
	s_and_b32 s2, s2, 1
	s_lshl_b32 s2, s2, 7
	s_add_i32 s2, s2, s12
	s_lshl_b32 s12, s10, 4
	s_add_i32 s14, s12, s2
	s_add_i32 s2, s14, 15
	s_branch .Lmy_lnm_go_0
.Lmy_lnm_old_0:
	s_lshl_b32 s2, s2, 3
	s_add_i32 s14, s10, s2
	s_movk_i32 s2, 0x7fff
.Lmy_lnm_go_0:
	s_waitcnt lgkmcnt(0)
	s_mov_b64 s[10:11], s[4:5]
	s_mov_b32 s4, s14
	s_cmpk_gt_u32 s4, 0x7fff
	s_cbranch_scc1 .LBB0_1086
	s_load_dwordx4 s[12:15], s[8:9], 0x90
	v_lshrrev_b32_e32 v18, 6, v18
	v_lshlrev_b32_e32 v2, 2, v34
	v_mov_b32_e32 v68, s4
	v_and_b32_e32 v36, 0xfc, v2
	v_mov_b32_e32 v67, 0
	v_lshlrev_b32_e32 v66, 11, v68
	v_lshlrev_b32_e32 v35, 2, v36
	v_lshl_add_u64 v[18:19], s[6:7], 0, v[66:67]
	v_lshlrev_b32_e32 v66, 1, v36
	s_waitcnt lgkmcnt(0)
	global_load_dwordx4 v[2:5], v35, s[12:13]
	global_load_dwordx4 v[6:9], v35, s[12:13] offset:1024
	global_load_dwordx4 v[10:13], v35, s[12:13] offset:2048
	global_load_dwordx4 v[14:17], v35, s[12:13] offset:3072
	v_lshl_add_u64 v[38:39], v[18:19], 0, v[66:67]
	global_load_dwordx4 v[18:21], v35, s[14:15]
	global_load_dwordx4 v[22:25], v35, s[14:15] offset:1024
	global_load_dwordx4 v[26:29], v35, s[14:15] offset:2048
	global_load_dwordx4 v[30:33], v35, s[14:15] offset:3072
	global_load_dwordx2 v[82:83], v[38:39], off offset:1536
	global_load_dwordx2 v[84:85], v[38:39], off offset:1024
	global_load_dwordx2 v[86:87], v[38:39], off offset:512
	global_load_dwordx2 v[88:89], v[38:39], off
	v_mov_b32_e32 v69, v67
	v_and_b32_e32 v34, 63, v34
	v_lshlrev_b64 v[70:71], 11, v[68:69]
	s_ashr_i32 s87, s86, 31
	v_lshl_or_b32 v70, v34, 3, v70
	v_lshl_add_u64 v[72:73], s[6:7], 0, v[66:67]
	v_lshlrev_b32_e32 v66, 2, v36
	v_mov_b32_e32 v91, -1
	s_mov_b64 s[12:13], 0
	s_mov_b32 s22, 0x8000
	s_mov_b64 s[14:15], 0x3000
	s_mov_b64 s[16:17], 0x4000
	v_mov_b32_e32 v90, 0x3727c5ac
	s_mov_b32 s23, 0x800000
	s_lshl_b64 s[18:19], s[86:87], 11
	s_mov_b32 s98, s86
	s_cmpk_lg_u32 s33, 0x100
	s_cbranch_scc1 .Lmy_lnm_st_a
	s_mov_b64 s[18:19], 0x800
	s_mov_b32 s98, 1
.Lmy_lnm_st_a:
	s_waitcnt vmcnt(0)
	v_mov_b64_e32 v[36:37], v[4:5]
	v_mov_b64_e32 v[44:45], v[8:9]
	v_mov_b64_e32 v[48:49], v[12:13]
	v_mov_b64_e32 v[56:57], v[16:17]
	v_mov_b64_e32 v[34:35], v[2:3]
	v_mov_b64_e32 v[42:43], v[6:7]
	v_mov_b64_e32 v[46:47], v[10:11]
	v_mov_b64_e32 v[54:55], v[14:15]
	v_mov_b32_e32 v38, v2
	v_mov_b32_e32 v39, v3
	v_mov_b32_e32 v40, v4
	v_mov_b32_e32 v41, v5
	v_mov_b32_e32 v50, v6
	v_mov_b32_e32 v51, v7
	v_mov_b32_e32 v52, v8
	v_mov_b32_e32 v53, v9
	v_mov_b32_e32 v58, v10
	v_mov_b32_e32 v59, v11
	v_mov_b32_e32 v60, v12
	v_mov_b32_e32 v61, v13
	v_mov_b32_e32 v62, v14
	v_mov_b32_e32 v63, v15
	v_mov_b32_e32 v64, v16
	v_mov_b32_e32 v65, v17
	s_branch .LBB0_1083

; DEVI float bflo(unsigned w) { return __uint_as_float(w << 16); }
; DEVI float bfhi(unsigned w) { return __uint_as_float(w & 0xffff0000u); }
; DEVI void phase_ln_mid(const Params& p, int l) {
;     ...
;     for (int t = gw; t < T_; t += nw) {
;         const int b = t >> 12; f32x4 v[4]; const int tn = t + nw < T_ ? t + nw : t;
; #pragma unroll
;         for (int i = 0; i < 4; ++i) { v[i] = (f32x4){bflo(rw[i].x), bfhi(rw[i].x), bflo(rw[i].y), bfhi(rw[i].y)}; rn[i] = *(const u32x2*)(xab + (size_t)tn * 1024 + lane * 4 + 256 * i); }
;         if (b != bcur) { bcur = b; const float* ad = p.ada + ((size_t)l * 8 + b) * 6144;
; #pragma unroll
;             for (int i = 0; i < 4; ++i) { sh4[i] = *(const f32x4*)(ad + 3072 + lane * 4 + 256 * i); sc4[i] = *(const f32x4*)(ad + 4096 + lane * 4 + 256 * i); } }
.LBB0_1083:
	v_mov_b32_e32 v69, v68
	v_add_u32_e32 v68, s98, v69
	v_cmp_gt_i32_e32 vcc, s22, v68
	s_nop 1
	v_cndmask_b32_e32 v74, v69, v68, vcc
	v_ashrrev_i32_e32 v75, 31, v74
	v_lshlrev_b64 v[74:75], 11, v[74:75]
	v_lshl_add_u64 v[92:93], v[72:73], 0, v[74:75]
	global_load_dwordx2 v[74:75], v[92:93], off
	global_load_dwordx2 v[76:77], v[92:93], off offset:512
	global_load_dwordx2 v[78:79], v[92:93], off offset:1024
	global_load_dwordx2 v[80:81], v[92:93], off offset:1536
	v_cmp_lt_i32_e32 vcc, s2, v68
	v_ashrrev_i32_e32 v69, 12, v69
	v_cmp_ne_u32_e64 s[4:5], v69, v91
	s_or_b64 s[12:13], vcc, s[12:13]
	s_and_saveexec_b64 s[20:21], s[4:5]
	s_cbranch_execz .LBB0_1082
	s_load_dwordx2 s[4:5], s[8:9], 0x108
	v_mul_hi_i32_i24_e32 v35, 0x6000, v69
	v_mul_i32_i24_e32 v34, 0x6000, v69
	v_mov_b32_e32 v91, v69
	s_waitcnt lgkmcnt(0)
	v_lshl_add_u64 v[34:35], s[4:5], 0, v[34:35]
	v_lshl_add_u64 v[34:35], v[34:35], 0, v[66:67]
	v_add_co_u32_e32 v96, vcc, 0x3000, v34
	v_lshl_add_u64 v[92:93], v[34:35], 0, s[14:15]
	s_nop 0
	v_addc_co_u32_e32 v97, vcc, 0, v35, vcc
	v_add_co_u32_e32 v98, vcc, 0x4000, v34
	v_lshl_add_u64 v[94:95], v[34:35], 0, s[16:17]
	s_nop 0
	v_addc_co_u32_e32 v99, vcc, 0, v35, vcc
	global_load_dwordx4 v[38:41], v[96:97], off
	global_load_dwordx4 v[34:37], v[98:99], off
	global_load_dwordx4 v[50:53], v[92:93], off offset:1024
	global_load_dwordx4 v[58:61], v[92:93], off offset:2048
	global_load_dwordx4 v[42:45], v[94:95], off offset:1024
	global_load_dwordx4 v[62:65], v[92:93], off offset:3072
	global_load_dwordx4 v[46:49], v[94:95], off offset:2048
	global_load_dwordx4 v[54:57], v[94:95], off offset:3072
	s_branch .LBB0_1082

; DEVI unsigned xb_add(unsigned* p, unsigned v) { return __hip_atomic_fetch_add(p, v, __ATOMIC_RELAXED, __HIP_MEMORY_SCOPE_AGENT); }
; DEVI void xcd_barrier(const XcdBarrier& b) {
;     asm volatile("s_waitcnt vmcnt(0)" ::: "memory");
;     __syncthreads();
;     if (threadIdx.x == 0) {
;         unsigned* bar = b.bar;
;         __builtin_amdgcn_s_waitcnt(0);
;         unsigned nloc = b.st[0], nx = b.st[1];
;         if (nloc == 0u) { xcd_barrier_complete(bar, b.x, nloc, nx); b.st[0] = nloc; b.st[1] = nx; }
;         const unsigned old = xb_add(&bar[XB_XSUB(b.x)], 1u);
;         const unsigned gen = old / nloc;
;         if (old + 1u == (gen + 1u) * nloc) {
.LBB0_1086:
	s_mov_b64 s[6:7], s[0:1]
	s_getreg_b32 s2, hwreg(HW_REG_XCC_ID, 0, 4)
	s_waitcnt vmcnt(0)
	s_waitcnt lgkmcnt(0)
	s_barrier
	s_cmpk_lg_u32 s33, 0x100
	s_cbranch_scc1 .Lmy_lnm_bar_0
	buffer_inv sc1
	s_mov_b64 s[4:5], exec
	s_branch .LBB0_1138
.Lmy_lnm_bar_0:
	s_mov_b64 s[4:5], exec
	v_readlane_b32 s8, v248, 0
	v_readlane_b32 s9, v248, 1
	s_and_b64 s[8:9], s[4:5], s[8:9]
	s_mov_b64 exec, s[8:9]
	s_cbranch_execz .LBB0_1138
	s_add_i32 s8, 0, 0x258f0
	v_mov_b32_e32 v2, s8
	s_load_dwordx2 s[6:7], s[6:7], 0xf8
	s_waitcnt vmcnt(0) expcnt(0) lgkmcnt(0)
	ds_read_b32 v4, v2
	s_add_i32 s8, 0, 0x258f4
	v_mov_b32_e32 v2, s8
	ds_read_b32 v2, v2
	s_and_b32 s2, s2, 15
	s_waitcnt lgkmcnt(1)
	v_cmp_ne_u32_e32 vcc, 0, v4
	s_cbranch_vccnz .LBB0_1102
	v_readlane_b32 s8, v248, 2
	v_readlane_b32 s9, v248, 3
	s_load_dwordx2 s[12:13], s[8:9], 0x4
	s_add_u32 s8, s6, 0x1000
	s_addc_u32 s9, s7, 0
	s_add_u32 s10, s6, 0x1100
	s_addc_u32 s11, s7, 0
	s_waitcnt lgkmcnt(0)
	s_mul_i32 s22, s12, s33
	s_add_u32 s12, s6, 0x1200
	s_mul_i32 s22, s22, s13
	s_addc_u32 s13, s7, 0
	s_add_u32 s14, s6, 0x1300
	s_addc_u32 s15, s7, 0
	s_mov_b32 s23, 1
	v_mov_b32_e32 v18, 0
	s_branch .LBB0_1090

; DEVI int vtid() { return tidx() & 255; }
; DEVI int vbid() { return bidx() * 2 + vhb(); }
; DEVI int vgrid() { return (int)gridDim.x * 2; }
; DEVI void phase_ln_mid(const Params& p, int l) {
;     const int lane = vtid() & 63, gw = vbid() * 4 + (vtid() >> 6), nw = vgrid() * 4;
;     bf16_t* xab = p.xa; bf16_t* hb = p.h; asm volatile("" : "+s"(xab), "+s"(hb));
;     f32x4 lg4[4], lb4[4], sh4[4], sc4[4]; int bcur = -1;
; #pragma unroll
;     for (int i = 0; i < 4; ++i) { const int c = lane * 4 + 256 * i; lg4[i] = *(const f32x4*)(p.ln1_g + l * 1024 + c); lb4[i] = *(const f32x4*)(p.ln1_b + l * 1024 + c); sh4[i] = lg4[i]; sc4[i] = lg4[i]; }
;     u32x2 rw[4], rn[4];
; #pragma unroll
;     for (int i = 0; i < 4; ++i) rw[i] = *(const u32x2*)(xab + (size_t)(gw < T_ ? gw : 0) * 1024 + lane * 4 + 256 * i);
;     for (int t = gw; t < T_; t += nw) {
.LBB0_2644:
	s_or_b64 exec, exec, s[4:5]
	s_mov_b64 s[6:7], s[0:1]
	s_waitcnt lgkmcnt(0)
	v_mov_b32_e32 v1, v0
	s_mov_b32 s2, s84
	v_mov_b32_e32 v2, v0
	s_barrier
	v_readfirstlane_b32 s4, v2
	s_lshr_b32 s14, s4, 6
	v_mov_b32_e32 v30, v0
	s_load_dwordx4 s[8:11], s[6:7], 0x160
	s_cmpk_lg_u32 s33, 0x100
	s_cbranch_scc1 .Lmy_lnm_old_1
	s_lshr_b32 s12, s2, 1
	s_and_b32 s13, s12, 7
	s_lshl_b32 s13, s13, 4
	s_lshr_b32 s12, s12, 3
	s_add_i32 s12, s12, s13
	s_lshl_b32 s12, s12, 8
	s_and_b32 s2, s2, 1
	s_lshl_b32 s2, s2, 7
	s_add_i32 s2, s2, s12
	s_lshl_b32 s12, s14, 4
	s_add_i32 s4, s12, s2
	s_add_i32 s2, s4, 15
	s_branch .Lmy_lnm_go_1
.Lmy_lnm_old_1:
	s_lshl_b32 s2, s2, 3
	s_add_i32 s4, s14, s2
	s_movk_i32 s2, 0x7fff
.Lmy_lnm_go_1:
	s_cmpk_gt_u32 s4, 0x7fff
	s_waitcnt lgkmcnt(0)
	s_cbranch_scc1 .LBB0_2650
	s_load_dwordx4 s[12:15], s[6:7], 0x90
	v_lshlrev_b32_e32 v2, 2, v1
	v_and_b32_e32 v34, 0xfc, v2
	v_lshlrev_b32_e32 v31, 2, v34
	v_or_b32_e32 v33, 0x800, v31
	s_waitcnt lgkmcnt(0)
	s_add_u32 s12, s12, 0x1000
	s_addc_u32 s13, s13, 0
	v_or_b32_e32 v35, 0xc00, v31
	v_lshrrev_b32_e32 v30, 6, v30
	v_or_b32_e32 v32, 0x400, v31
	global_load_dwordx4 v[2:5], v31, s[12:13]
	global_load_dwordx4 v[6:9], v32, s[12:13]
	global_load_dwordx4 v[10:13], v33, s[12:13]
	global_load_dwordx4 v[14:17], v35, s[12:13]
	s_add_u32 s12, s14, 0x1000
	v_mov_b32_e32 v68, s4
	s_addc_u32 s13, s15, 0
	v_mov_b32_e32 v67, 0
	v_lshlrev_b32_e32 v66, 11, v68
	global_load_dwordx4 v[18:21], v31, s[12:13]
	global_load_dwordx4 v[22:25], v32, s[12:13]
	global_load_dwordx4 v[26:29], v33, s[12:13]
	v_lshl_add_u64 v[30:31], s[10:11], 0, v[66:67]
	v_lshlrev_b32_e32 v66, 1, v34
	v_lshl_add_u64 v[36:37], v[30:31], 0, v[66:67]
	global_load_dwordx2 v[82:83], v[36:37], off offset:1536
	global_load_dwordx2 v[84:85], v[36:37], off offset:1024
	global_load_dwordx2 v[86:87], v[36:37], off offset:512
	global_load_dwordx2 v[88:89], v[36:37], off
	global_load_dwordx4 v[30:33], v35, s[12:13]
	v_mov_b32_e32 v69, v67
	v_and_b32_e32 v35, 63, v1
	v_lshlrev_b64 v[70:71], 11, v[68:69]
	v_lshl_or_b32 v70, v35, 3, v70
	v_lshl_add_u64 v[72:73], s[10:11], 0, v[66:67]
	v_lshlrev_b32_e32 v66, 2, v34
	s_ashr_i32 s87, s86, 31
	v_mov_b32_e32 v90, -1
	s_mov_b64 s[12:13], 0
	s_mov_b32 s22, 0x8000
	s_mov_b64 s[14:15], 0x3000
	s_mov_b64 s[16:17], 0x4000
	v_mov_b32_e32 v1, 0x3727c5ac
	s_mov_b32 s23, 0x800000
	s_lshl_b64 s[18:19], s[86:87], 11
	s_mov_b32 s98, s86
	s_cmpk_lg_u32 s33, 0x100
	s_cbranch_scc1 .Lmy_lnm_st_b
	s_mov_b64 s[18:19], 0x800
	s_mov_b32 s98, 1

; DEVI float bflo(unsigned w) { return __uint_as_float(w << 16); }
; DEVI float bfhi(unsigned w) { return __uint_as_float(w & 0xffff0000u); }
; DEVI void phase_ln_mid(const Params& p, int l) {
;     ...
;     for (int t = gw; t < T_; t += nw) {
;         const int b = t >> 12; f32x4 v[4]; const int tn = t + nw < T_ ? t + nw : t;
; #pragma unroll
;         for (int i = 0; i < 4; ++i) { v[i] = (f32x4){bflo(rw[i].x), bfhi(rw[i].x), bflo(rw[i].y), bfhi(rw[i].y)}; rn[i] = *(const u32x2*)(xab + (size_t)tn * 1024 + lane * 4 + 256 * i); }
;         if (b != bcur) { bcur = b; const float* ad = p.ada + ((size_t)l * 8 + b) * 6144;
; #pragma unroll
;             for (int i = 0; i < 4; ++i) { sh4[i] = *(const f32x4*)(ad + 3072 + lane * 4 + 256 * i); sc4[i] = *(const f32x4*)(ad + 4096 + lane * 4 + 256 * i); } }
.LBB0_2647:
	v_mov_b32_e32 v69, v68
	v_add_u32_e32 v68, s98, v69
	v_cmp_gt_i32_e32 vcc, s22, v68
	s_nop 1
	v_cndmask_b32_e32 v74, v69, v68, vcc
	v_ashrrev_i32_e32 v75, 31, v74
	v_lshlrev_b64 v[74:75], 11, v[74:75]
	v_lshl_add_u64 v[92:93], v[72:73], 0, v[74:75]
	global_load_dwordx2 v[74:75], v[92:93], off
	global_load_dwordx2 v[76:77], v[92:93], off offset:512
	global_load_dwordx2 v[78:79], v[92:93], off offset:1024
	global_load_dwordx2 v[80:81], v[92:93], off offset:1536
	v_cmp_lt_i32_e32 vcc, s2, v68
	v_ashrrev_i32_e32 v69, 12, v69
	v_cmp_ne_u32_e64 s[4:5], v69, v90
	s_or_b64 s[12:13], vcc, s[12:13]
	s_and_saveexec_b64 s[20:21], s[4:5]
	s_cbranch_execz .LBB0_2646
	s_load_dwordx2 s[4:5], s[6:7], 0x108
	v_add_u32_e32 v34, 8, v69
	v_mul_hi_i32_i24_e32 v35, 0x6000, v34
	v_mul_i32_i24_e32 v34, 0x6000, v34
	s_waitcnt lgkmcnt(0)
	v_lshl_add_u64 v[34:35], s[4:5], 0, v[34:35]
	v_lshl_add_u64 v[34:35], v[34:35], 0, v[66:67]
	v_add_co_u32_e32 v94, vcc, 0x3000, v34
	v_lshl_add_u64 v[90:91], v[34:35], 0, s[14:15]
	s_nop 0
	v_addc_co_u32_e32 v95, vcc, 0, v35, vcc
	v_add_co_u32_e32 v96, vcc, 0x4000, v34
	v_lshl_add_u64 v[92:93], v[34:35], 0, s[16:17]
	s_nop 0
	v_addc_co_u32_e32 v97, vcc, 0, v35, vcc
	global_load_dwordx4 v[38:41], v[94:95], off
	global_load_dwordx4 v[34:37], v[96:97], off
	global_load_dwordx4 v[50:53], v[90:91], off offset:1024
	global_load_dwordx4 v[58:61], v[90:91], off offset:2048
	global_load_dwordx4 v[42:45], v[92:93], off offset:1024
	global_load_dwordx4 v[62:65], v[90:91], off offset:3072
	global_load_dwordx4 v[46:49], v[92:93], off offset:2048
	global_load_dwordx4 v[54:57], v[92:93], off offset:3072
	v_mov_b32_e32 v90, v69
	s_branch .LBB0_2646

; DEVI unsigned xb_ld(unsigned* p)              { return __hip_atomic_load(p, __ATOMIC_RELAXED, __HIP_MEMORY_SCOPE_AGENT); }
; DEVI unsigned xb_add(unsigned* p, unsigned v) { return __hip_atomic_fetch_add(p, v, __ATOMIC_RELAXED, __HIP_MEMORY_SCOPE_AGENT); }
; DEVI void xcd_barrier_complete(unsigned* bar, unsigned x, unsigned& nloc, unsigned& nx) {
;     const unsigned G = gridDim.x * gridDim.y * gridDim.z;
;     unsigned sum, cnt, mine, sp = 0u;
;     for (;;) {
;         sum = 0u; cnt = 0u; mine = 0u;
; #pragma unroll
;         for (unsigned j = 0; j < 16; ++j) { const unsigned c = xb_ld(&bar[XB_XCNT(j)]); sum += c; cnt += (c > 0u) ? 1u : 0u; mine = (j == x) ? c : mine; }
; DEVI void xcd_barrier(const XcdBarrier& b) {
;     asm volatile("s_waitcnt vmcnt(0)" ::: "memory");
;     __syncthreads();
;     if (threadIdx.x == 0) {
;         unsigned* bar = b.bar;
;         __builtin_amdgcn_s_waitcnt(0);
;         unsigned nloc = b.st[0], nx = b.st[1];
;         if (nloc == 0u) { xcd_barrier_complete(bar, b.x, nloc, nx); b.st[0] = nloc; b.st[1] = nx; }
;         const unsigned old = xb_add(&bar[XB_XSUB(b.x)], 1u);
.Lmy_lnm_bar_1:
	s_mov_b64 s[4:5], exec
	v_readlane_b32 s8, v248, 0
	v_readlane_b32 s9, v248, 1
	s_and_b64 s[8:9], s[4:5], s[8:9]
	s_mov_b64 exec, s[8:9]
	s_cbranch_execz .LBB0_2702
	s_add_i32 s8, 0, 0x258f0
	v_mov_b32_e32 v1, s8
	s_load_dwordx2 s[6:7], s[6:7], 0xf8
	s_waitcnt vmcnt(0) expcnt(0) lgkmcnt(0)
	ds_read_b32 v3, v1
	s_add_i32 s8, 0, 0x258f4
	v_mov_b32_e32 v1, s8
	ds_read_b32 v1, v1
	s_and_b32 s2, s2, 15
	s_waitcnt lgkmcnt(1)
	v_cmp_ne_u32_e32 vcc, 0, v3
	s_cbranch_vccnz .LBB0_2666
	v_readlane_b32 s8, v248, 2
	v_readlane_b32 s9, v248, 3
	s_load_dwordx2 s[12:13], s[8:9], 0x4
	s_add_u32 s8, s6, 0x1000
	s_addc_u32 s9, s7, 0
	s_add_u32 s10, s6, 0x1100
	s_addc_u32 s11, s7, 0
	s_waitcnt lgkmcnt(0)
	s_mul_i32 s22, s12, s33
	s_add_u32 s12, s6, 0x1200
	s_mul_i32 s22, s22, s13
	s_addc_u32 s13, s7, 0
	s_add_u32 s14, s6, 0x1300
	s_addc_u32 s15, s7, 0
	s_mov_b32 s23, 1
	v_mov_b32_e32 v17, 0
	s_branch .LBB0_2654
